# QKV-GEMM epilogue: the 8 serialised rstd load groups software-pipelined two deep with a second register set
# speedup vs baseline: 1.0064x; 1.0064x over previous
; __device__ __forceinline__ void load_rstd(const float* ss, int rowb, int fq, float (&rs)[2][4]) {
; #pragma unroll
;     for (int ai = 0; ai < 2; ++ai)
; #pragma unroll
;         for (int m = 0; m < 4; ++m) {
;             const f32x4* p = (const f32x4*)(ss + (size_t)(rowb + ai * HALF + m * 16) * 32 + fq * 8);
;             const f32x4 a = p[0], b = p[1];
;             float s = ((a[0] + a[1]) + (a[2] + a[3])) + ((b[0] + b[1]) + (b[2] + b[3]));
;             s += __shfl_xor(s, 16); s += __shfl_xor(s, 32);
;             rs[ai][m] = __builtin_amdgcn_rsqf(s * (1.0f / D) + EPS);
;         }
;     __device__ __forceinline__ void operator()(const f32x4 (&acc)[2][2][4][2], const Unit& u, int wr, int wc, int fr, int fq, int ui) const {
;         const int ct = u.pn * BM; const int cb = ct + wc * 32 + 8 * fq;
;         f32x4 bv[2][2];
; #pragma unroll
;         for (int bj = 0; bj < 2; ++bj)
; #pragma unroll
;             for (int n = 0; n < 2; ++n) bv[bj][n] = *(const f32x4*)(bias + cb + bj * HALF + 4 * n);
;         float rs[2][4]; load_rstd(ss, u.pm * BM + wr * 64 + fr, fq, rs);
.LBB0_345:
	v_and_b32_e32 v147, 64, v228
	v_xor_b32_e32 v146, 16, v228
	v_add_u32_e32 v213, 64, v147
	v_cmp_lt_i32_e32 vcc, v146, v213
	s_lshl_b32 s43, s8, 8
	v_lshl_add_u32 v180, s42, 8, v163
	v_cndmask_b32_e32 v146, v228, v146, vcc
	v_lshlrev_b32_e32 v211, 2, v146
	v_xor_b32_e32 v146, 32, v228
	v_cmp_lt_i32_e32 vcc, v146, v213
	v_or_b32_e32 v186, s43, v162
	v_ashrrev_i32_e32 v181, 31, v180
	v_cndmask_b32_e32 v146, v228, v146, vcc
	v_ashrrev_i32_e32 v187, 31, v186
	v_lshlrev_b32_e32 v212, 2, v146
	v_lshlrev_b64 v[146:147], 7, v[180:181]
	v_lshl_add_u64 v[52:53], v[186:187], 2, s[30:31]
	v_lshl_add_u64 v[150:151], v[164:165], 0, v[146:147]
	global_load_dwordx4 v[64:67], v[52:53], off offset:16
	global_load_dwordx4 v[68:71], v[52:53], off
	global_load_dwordx4 v[48:51], v[52:53], off offset:528
	s_nop 0
	global_load_dwordx4 v[52:55], v[52:53], off offset:512
	s_nop 0
	global_load_dwordx4 v[146:149], v[150:151], off
	s_nop 0
	global_load_dwordx4 v[150:153], v[150:151], off offset:16
	v_or_b32_e32 v204, 16, v180
	v_ashrrev_i32_e32 v205, 31, v204
	v_or_b32_e32 v202, 32, v180
	v_ashrrev_i32_e32 v203, 31, v202
	v_or_b32_e32 v200, 48, v180
	v_ashrrev_i32_e32 v201, 31, v200
	v_add_u32_e32 v198, 0x80, v180
	v_ashrrev_i32_e32 v199, 31, v198
	v_add_u32_e32 v188, 0x90, v180
	v_ashrrev_i32_e32 v189, 31, v188
	v_add_u32_e32 v184, 0xa0, v180
	v_ashrrev_i32_e32 v185, 31, v184
	v_add_u32_e32 v182, 0xb0, v180
	v_ashrrev_i32_e32 v183, 31, v182
	s_cmp_gt_i32 s8, 7
	s_cselect_b64 s[8:9], -1, 0
	s_cmp_lt_i32 s43, s72
	s_cselect_b64 s[10:11], -1, 0
	s_and_b64 s[12:13], s[8:9], s[10:11]
	s_and_b64 s[52:53], s[12:13], s[36:37]
	s_and_b64 vcc, exec, s[52:53]
	s_mov_b32 s79, 0xff800000
	s_waitcnt vmcnt(0)
	v_mov_b32_e32 v166, v146
	v_mov_b32_e32 v167, v150
	v_mov_b32_e32 v150, v147
	v_pk_add_f32 v[146:147], v[166:167], v[150:151]
	v_mov_b32_e32 v150, v148
	v_mov_b32_e32 v151, v152
	v_mov_b32_e32 v152, v149
	v_pk_add_f32 v[148:149], v[150:151], v[152:153]
	s_nop 0
	v_pk_add_f32 v[146:147], v[146:147], v[148:149]
	s_nop 0
	v_add_f32_e32 v146, v146, v147
	ds_bpermute_b32 v147, v211, v146
	s_waitcnt lgkmcnt(0)
	v_add_f32_e32 v146, v146, v147
	ds_bpermute_b32 v147, v212, v146
	s_waitcnt lgkmcnt(0)
	v_add_f32_e32 v146, v146, v147
	v_fmamk_f32 v146, v146, 0x3a000000, v229
	v_rsq_f32_e32 v194, v146
	v_lshlrev_b64 v[146:147], 7, v[204:205]
	v_lshl_add_u64 v[150:151], v[164:165], 0, v[146:147]
	global_load_dwordx4 v[146:149], v[150:151], off offset:16
	s_nop 0
	global_load_dwordx4 v[150:153], v[150:151], off
	v_lshlrev_b64 v[190:191], 7, v[202:203]
	v_lshl_add_u64 v[206:207], v[164:165], 0, v[190:191]
	global_load_dwordx4 v[190:193], v[206:207], off offset:16
	s_nop 0
	global_load_dwordx4 v[206:209], v[206:207], off
	s_waitcnt vmcnt(3)
	v_add_f32_e32 v146, v146, v147
	s_waitcnt vmcnt(2)
	v_add_f32_e32 v150, v150, v151
	v_add_f32_e32 v151, v152, v153
	v_add_f32_e32 v147, v148, v149
	v_add_f32_e32 v150, v150, v151
	v_add_f32_e32 v146, v146, v147
	v_add_f32_e32 v146, v150, v146
	ds_bpermute_b32 v147, v211, v146
	s_waitcnt lgkmcnt(0)
	v_add_f32_e32 v226, v146, v147
	v_lshlrev_b64 v[146:147], 7, v[200:201]
	v_lshl_add_u64 v[150:151], v[164:165], 0, v[146:147]
	global_load_dwordx4 v[146:149], v[150:151], off offset:16
	s_nop 0
	global_load_dwordx4 v[150:153], v[150:151], off
	ds_bpermute_b32 v227, v212, v226
	s_waitcnt vmcnt(3)
	v_add_f32_e32 v190, v190, v191
	s_waitcnt vmcnt(2)
	v_add_f32_e32 v206, v206, v207
	v_add_f32_e32 v207, v208, v209
	v_add_f32_e32 v191, v192, v193
	v_add_f32_e32 v206, v206, v207
	v_add_f32_e32 v190, v190, v191
	v_add_f32_e32 v190, v206, v190
	ds_bpermute_b32 v191, v211, v190
	s_waitcnt lgkmcnt(0)
	v_add_f32_e32 v224, v190, v191
	v_lshlrev_b64 v[190:191], 7, v[198:199]
	v_lshl_add_u64 v[206:207], v[164:165], 0, v[190:191]
	global_load_dwordx4 v[190:193], v[206:207], off offset:16
	s_nop 0
	global_load_dwordx4 v[206:209], v[206:207], off
	ds_bpermute_b32 v225, v212, v224
	s_waitcnt vmcnt(3)
	v_add_f32_e32 v146, v146, v147
	s_waitcnt vmcnt(2)
	v_add_f32_e32 v150, v150, v151
	v_add_f32_e32 v151, v152, v153
	v_add_f32_e32 v147, v148, v149
	v_add_f32_e32 v150, v150, v151
	v_add_f32_e32 v146, v146, v147
	v_add_f32_e32 v146, v150, v146
	ds_bpermute_b32 v147, v211, v146
	s_waitcnt lgkmcnt(0)
	v_add_f32_e32 v222, v146, v147
	v_lshlrev_b64 v[146:147], 7, v[188:189]
	v_lshl_add_u64 v[150:151], v[164:165], 0, v[146:147]
	global_load_dwordx4 v[146:149], v[150:151], off offset:16
	s_nop 0
	global_load_dwordx4 v[150:153], v[150:151], off
	ds_bpermute_b32 v223, v212, v222
	s_waitcnt vmcnt(3)
	v_add_f32_e32 v190, v190, v191
	s_waitcnt vmcnt(2)
	v_add_f32_e32 v206, v206, v207
	v_add_f32_e32 v207, v208, v209
	v_add_f32_e32 v191, v192, v193
	v_add_f32_e32 v206, v206, v207
	v_add_f32_e32 v190, v190, v191
	v_add_f32_e32 v190, v206, v190
	ds_bpermute_b32 v191, v211, v190
	s_waitcnt lgkmcnt(0)
	v_add_f32_e32 v220, v190, v191
	v_lshlrev_b64 v[190:191], 7, v[184:185]
	v_lshl_add_u64 v[206:207], v[164:165], 0, v[190:191]
	global_load_dwordx4 v[190:193], v[206:207], off offset:16
	s_nop 0
	global_load_dwordx4 v[206:209], v[206:207], off
	ds_bpermute_b32 v221, v212, v220
	s_waitcnt vmcnt(3)
	v_add_f32_e32 v146, v146, v147
	s_waitcnt vmcnt(2)
	v_add_f32_e32 v150, v150, v151
	v_add_f32_e32 v151, v152, v153
	v_add_f32_e32 v147, v148, v149
	v_add_f32_e32 v150, v150, v151
	v_add_f32_e32 v146, v146, v147
	v_add_f32_e32 v146, v150, v146
	ds_bpermute_b32 v147, v211, v146
	s_waitcnt lgkmcnt(0)
	v_add_f32_e32 v216, v146, v147
	v_lshlrev_b64 v[146:147], 7, v[182:183]
	v_lshl_add_u64 v[150:151], v[164:165], 0, v[146:147]
	global_load_dwordx4 v[146:149], v[150:151], off offset:16
	s_nop 0
	global_load_dwordx4 v[150:153], v[150:151], off
	ds_bpermute_b32 v218, v212, v216
	s_waitcnt vmcnt(3)
	v_add_f32_e32 v190, v190, v191
	s_waitcnt vmcnt(2)
	v_add_f32_e32 v206, v206, v207
	v_add_f32_e32 v207, v208, v209
	v_add_f32_e32 v191, v192, v193
	v_add_f32_e32 v206, v206, v207
	v_add_f32_e32 v190, v190, v191
	v_add_f32_e32 v190, v206, v190
	ds_bpermute_b32 v191, v211, v190
	s_waitcnt lgkmcnt(0)
	v_add_f32_e32 v214, v190, v191
	ds_bpermute_b32 v215, v212, v214
	s_waitcnt vmcnt(1)
	v_add_f32_e32 v146, v146, v147
	s_waitcnt vmcnt(0)
	v_add_f32_e32 v150, v150, v151
	v_add_f32_e32 v151, v152, v153
	v_add_f32_e32 v147, v148, v149
	v_add_f32_e32 v150, v150, v151
	v_add_f32_e32 v146, v146, v147
	v_add_f32_e32 v146, v150, v146
	ds_bpermute_b32 v147, v211, v146
	v_pk_fma_f32 v[148:149], v[144:145], v[194:195], v[70:71] op_sel_hi:[1,0,1]
	v_pk_fma_f32 v[150:151], v[142:143], v[194:195], v[68:69] op_sel_hi:[1,0,1]
	v_pk_fma_f32 v[144:145], v[140:141], v[194:195], v[66:67] op_sel_hi:[1,0,1]
	s_waitcnt lgkmcnt(0)
	v_add_f32_e32 v217, v146, v147
	ds_bpermute_b32 v219, v212, v217
	v_pk_fma_f32 v[146:147], v[138:139], v[194:195], v[64:65] op_sel_hi:[1,0,1]
	s_cbranch_vccz .LBB0_347
;     __device__ __forceinline__ void operator()(const f32x4 (&acc)[2][2][4][2], const Unit& u, int wr, int wc, int fr, int fq, int ui) const {
;     ...
;                     const f32x4 v0 = acc[ai][bj][m][0] * r + bv[bj][0], v1 = acc[ai][bj][m][1] * r + bv[bj][1];
;                     csum[bj][0] += v0; csum[bj][1] += v1;
;                     if (do_km) kmx[bj] = fmaxf(kmx[bj], fmaxf(fmaxf(fmaxf(fabsf(v0[0]), fabsf(v0[1])), fmaxf(fabsf(v0[2]), fabsf(v0[3]))), fmaxf(fmaxf(fabsf(v1[0]), fabsf(v1[1])), fmaxf(fabsf(v1[2]), fabsf(v1[3])))));
	v_max_f32_e64 v138, |v149|, |v149|
	v_max_f32_e64 v139, |v148|, |v148|
	v_max_f32_e32 v138, v139, v138
	v_max_f32_e64 v139, |v145|, |v145|
	v_max_f32_e64 v140, |v144|, |v144|
	v_max_f32_e32 v139, v140, v139
	v_max3_f32 v138, |v150|, |v151|, v138
	v_max3_f32 v139, |v146|, |v147|, v139
	v_max3_f32 v152, v138, v139, 0
	s_branch .LBB0_348
